# combined + XATT O-tile store: row sums read as 4 b128, 16 rcp, staged bf16 writes batched, one wait
# speedup vs baseline: 1.0048x; 1.0048x over previous
; #define LAS __attribute__((address_space(3)))
; __device__ __forceinline__ bf16 f2bf(float f) { return (bf16)cvt_pk_bf16(f, f); }
; __device__ __forceinline__ int crow(int r, int hi) { return (r & 3) + 8 * (r >> 2) + 4 * hi; }
;     __device__ __forceinline__ bf16* out_ptr(int w, int row) const { return zo ? zo + (size_t)((i0 + 32 * w + row) * dil + r) * D + h * 128 : z + rowoff(i0 + 32 * w + row); }
; template <int DV32, bool WT, class P>
; __device__ __forceinline__ void store_o_tile(LAS unsigned char* stg, const f32x16 (&o)[DV32], const LAS float* li_l, const P& c, int w, int lane) {
;     const int r32 = lane & 31, hi = lane >> 5; constexpr int PITCH = 64 * DV32;
; #pragma unroll
;     for (int r = 0; r < 16; ++r) { const int orow = crow(r, hi); const float rl = __builtin_amdgcn_rcpf(li_l[orow]);
; #pragma unroll
;         for (int d = 0; d < DV32; ++d) *(LAS bf16*)(stg + orow * PITCH + (d * 32 + r32) * 2) = f2bf(o[d][r] * rl); }
;     asm volatile("s_waitcnt lgkmcnt(0)" ::: "memory");
;     constexpr int CPR = PITCH / 16;
; #pragma unroll
;     for (int i = 0; i < (32 * CPR) / 64; ++i) { const int idx = lane + 64 * i, row = idx / CPR, ch = idx % CPR;
;         const u32x4 v = *(const LAS u32x4*)(stg + row * PITCH + ch * 16); bf16* gp = c.out_ptr(w, row) + ch * 8;
;         if constexpr (WT) { if (c.wt) asm volatile("global_store_dwordx4 %0, %1, off sc1\n\ts_nop 1" :: "v"(gp), "v"(v) : "memory");     else *(u32x4*)gp = v; }
;         else *(u32x4*)gp = v; }
.LBB0_1216:
	s_or_b64 exec, exec, s[0:1]
	v_lshrrev_b32_e32 v64, 3, v155
	v_and_b32_e32 v66, 4, v64
	s_waitcnt lgkmcnt(0)
	v_lshl_add_u32 v67, v66, 2, s10
	ds_read_b128 v[70:73], v67
	ds_read_b128 v[74:77], v67 offset:32
	ds_read_b128 v[78:81], v67 offset:64
	ds_read_b128 v[82:85], v67 offset:96
	s_lshl_b32 s4, s11, 13
	s_addk_i32 s4, 0x100
	v_and_b32_e32 v69, 62, v160
	v_add_u32_e32 v69, s4, v69
	v_lshl_add_u32 v66, v66, 8, v69
	s_waitcnt lgkmcnt(0)
	v_rcp_f32_e32 v70, v70
	v_rcp_f32_e32 v71, v71
	v_rcp_f32_e32 v72, v72
	v_rcp_f32_e32 v73, v73
	v_rcp_f32_e32 v74, v74
	v_rcp_f32_e32 v75, v75
	v_rcp_f32_e32 v76, v76
	v_rcp_f32_e32 v77, v77
	v_rcp_f32_e32 v78, v78
	v_rcp_f32_e32 v79, v79
	v_rcp_f32_e32 v80, v80
	v_rcp_f32_e32 v81, v81
	v_rcp_f32_e32 v82, v82
	v_rcp_f32_e32 v83, v83
	v_rcp_f32_e32 v84, v84
	v_rcp_f32_e32 v85, v85
	v_mul_f32_e32 v16, v16, v70
	v_cvt_pk_bf16_f32 v16, v16, v16
	ds_write_b16 v66, v16
	v_mul_f32_e32 v32, v32, v70
	v_cvt_pk_bf16_f32 v32, v32, v32
	ds_write_b16 v66, v32 offset:64
	v_mul_f32_e32 v48, v48, v70
	v_cvt_pk_bf16_f32 v48, v48, v48
	ds_write_b16 v66, v48 offset:128
	v_mul_f32_e32 v0, v0, v70
	v_cvt_pk_bf16_f32 v0, v0, v0
	ds_write_b16 v66, v0 offset:192
	v_mul_f32_e32 v17, v17, v71
	v_cvt_pk_bf16_f32 v17, v17, v17
	ds_write_b16 v66, v17 offset:256
	v_mul_f32_e32 v33, v33, v71
	v_cvt_pk_bf16_f32 v33, v33, v33
	ds_write_b16 v66, v33 offset:320
	v_mul_f32_e32 v49, v49, v71
	v_cvt_pk_bf16_f32 v49, v49, v49
	ds_write_b16 v66, v49 offset:384
	v_mul_f32_e32 v1, v1, v71
	v_cvt_pk_bf16_f32 v1, v1, v1
	ds_write_b16 v66, v1 offset:448
	v_mul_f32_e32 v18, v18, v72
	v_cvt_pk_bf16_f32 v18, v18, v18
	ds_write_b16 v66, v18 offset:512
	v_mul_f32_e32 v34, v34, v72
	v_cvt_pk_bf16_f32 v34, v34, v34
	ds_write_b16 v66, v34 offset:576
	v_mul_f32_e32 v50, v50, v72
	v_cvt_pk_bf16_f32 v50, v50, v50
	ds_write_b16 v66, v50 offset:640
	v_mul_f32_e32 v2, v2, v72
	v_cvt_pk_bf16_f32 v2, v2, v2
	ds_write_b16 v66, v2 offset:704
	v_mul_f32_e32 v19, v19, v73
	v_cvt_pk_bf16_f32 v19, v19, v19
	ds_write_b16 v66, v19 offset:768
	v_mul_f32_e32 v35, v35, v73
	v_cvt_pk_bf16_f32 v35, v35, v35
	ds_write_b16 v66, v35 offset:832
	v_mul_f32_e32 v51, v51, v73
	v_cvt_pk_bf16_f32 v51, v51, v51
	ds_write_b16 v66, v51 offset:896
	v_mul_f32_e32 v3, v3, v73
	v_cvt_pk_bf16_f32 v3, v3, v3
	ds_write_b16 v66, v3 offset:960
	v_mul_f32_e32 v20, v20, v74
	v_cvt_pk_bf16_f32 v20, v20, v20
	ds_write_b16 v66, v20 offset:2048
	v_mul_f32_e32 v36, v36, v74
	v_cvt_pk_bf16_f32 v36, v36, v36
	ds_write_b16 v66, v36 offset:2112
	v_mul_f32_e32 v52, v52, v74
	v_cvt_pk_bf16_f32 v52, v52, v52
	ds_write_b16 v66, v52 offset:2176
	v_mul_f32_e32 v4, v4, v74
	v_cvt_pk_bf16_f32 v4, v4, v4
	ds_write_b16 v66, v4 offset:2240
	v_mul_f32_e32 v21, v21, v75
	v_cvt_pk_bf16_f32 v21, v21, v21
	ds_write_b16 v66, v21 offset:2304
	v_mul_f32_e32 v37, v37, v75
	v_cvt_pk_bf16_f32 v37, v37, v37
	ds_write_b16 v66, v37 offset:2368
	v_mul_f32_e32 v53, v53, v75
	v_cvt_pk_bf16_f32 v53, v53, v53
	ds_write_b16 v66, v53 offset:2432
	v_mul_f32_e32 v5, v5, v75
	v_cvt_pk_bf16_f32 v5, v5, v5
	ds_write_b16 v66, v5 offset:2496
	v_mul_f32_e32 v22, v22, v76
	v_cvt_pk_bf16_f32 v22, v22, v22
	ds_write_b16 v66, v22 offset:2560
	v_mul_f32_e32 v38, v38, v76
	v_cvt_pk_bf16_f32 v38, v38, v38
	ds_write_b16 v66, v38 offset:2624
	v_mul_f32_e32 v54, v54, v76
	v_cvt_pk_bf16_f32 v54, v54, v54
	ds_write_b16 v66, v54 offset:2688
	v_mul_f32_e32 v6, v6, v76
	v_cvt_pk_bf16_f32 v6, v6, v6
	ds_write_b16 v66, v6 offset:2752
	v_mul_f32_e32 v23, v23, v77
	v_cvt_pk_bf16_f32 v23, v23, v23
	ds_write_b16 v66, v23 offset:2816
	v_mul_f32_e32 v39, v39, v77
	v_cvt_pk_bf16_f32 v39, v39, v39
	ds_write_b16 v66, v39 offset:2880
	v_mul_f32_e32 v55, v55, v77
	v_cvt_pk_bf16_f32 v55, v55, v55
	ds_write_b16 v66, v55 offset:2944
	v_mul_f32_e32 v7, v7, v77
	v_cvt_pk_bf16_f32 v7, v7, v7
; #define LAS __attribute__((address_space(3)))
; __device__ __forceinline__ bf16 f2bf(float f) { return (bf16)cvt_pk_bf16(f, f); }
; __device__ __forceinline__ int crow(int r, int hi) { return (r & 3) + 8 * (r >> 2) + 4 * hi; }
;     __device__ __forceinline__ bf16* out_ptr(int w, int row) const { return zo ? zo + (size_t)((i0 + 32 * w + row) * dil + r) * D + h * 128 : z + rowoff(i0 + 32 * w + row); }
; template <int DV32, bool WT, class P>
; __device__ __forceinline__ void store_o_tile(LAS unsigned char* stg, const f32x16 (&o)[DV32], const LAS float* li_l, const P& c, int w, int lane) {
;     const int r32 = lane & 31, hi = lane >> 5; constexpr int PITCH = 64 * DV32;
; #pragma unroll
;     for (int r = 0; r < 16; ++r) { const int orow = crow(r, hi); const float rl = __builtin_amdgcn_rcpf(li_l[orow]);
; #pragma unroll
;         for (int d = 0; d < DV32; ++d) *(LAS bf16*)(stg + orow * PITCH + (d * 32 + r32) * 2) = f2bf(o[d][r] * rl); }
;     asm volatile("s_waitcnt lgkmcnt(0)" ::: "memory");
;     constexpr int CPR = PITCH / 16;
; #pragma unroll
;     for (int i = 0; i < (32 * CPR) / 64; ++i) { const int idx = lane + 64 * i, row = idx / CPR, ch = idx % CPR;
;         const u32x4 v = *(const LAS u32x4*)(stg + row * PITCH + ch * 16); bf16* gp = c.out_ptr(w, row) + ch * 8;
;         if constexpr (WT) { if (c.wt) asm volatile("global_store_dwordx4 %0, %1, off sc1\n\ts_nop 1" :: "v"(gp), "v"(v) : "memory");     else *(u32x4*)gp = v; }
;         else *(u32x4*)gp = v; }
	ds_write_b16 v66, v7 offset:3008
	v_mul_f32_e32 v24, v24, v78
	v_cvt_pk_bf16_f32 v24, v24, v24
	ds_write_b16 v66, v24 offset:4096
	v_mul_f32_e32 v40, v40, v78
	v_cvt_pk_bf16_f32 v40, v40, v40
	ds_write_b16 v66, v40 offset:4160
	v_mul_f32_e32 v56, v56, v78
	v_cvt_pk_bf16_f32 v56, v56, v56
	ds_write_b16 v66, v56 offset:4224
	v_mul_f32_e32 v8, v8, v78
	v_cvt_pk_bf16_f32 v8, v8, v8
	ds_write_b16 v66, v8 offset:4288
	v_mul_f32_e32 v25, v25, v79
	v_cvt_pk_bf16_f32 v25, v25, v25
	ds_write_b16 v66, v25 offset:4352
	v_mul_f32_e32 v41, v41, v79
	v_cvt_pk_bf16_f32 v41, v41, v41
	ds_write_b16 v66, v41 offset:4416
	v_mul_f32_e32 v57, v57, v79
	v_cvt_pk_bf16_f32 v57, v57, v57
	ds_write_b16 v66, v57 offset:4480
	v_mul_f32_e32 v9, v9, v79
	v_cvt_pk_bf16_f32 v9, v9, v9
	ds_write_b16 v66, v9 offset:4544
	v_mul_f32_e32 v26, v26, v80
	v_cvt_pk_bf16_f32 v26, v26, v26
	ds_write_b16 v66, v26 offset:4608
	v_mul_f32_e32 v42, v42, v80
	v_cvt_pk_bf16_f32 v42, v42, v42
	ds_write_b16 v66, v42 offset:4672
	v_mul_f32_e32 v58, v58, v80
	v_cvt_pk_bf16_f32 v58, v58, v58
	ds_write_b16 v66, v58 offset:4736
	v_mul_f32_e32 v10, v10, v80
	v_cvt_pk_bf16_f32 v10, v10, v10
	ds_write_b16 v66, v10 offset:4800
	v_mul_f32_e32 v27, v27, v81
	v_cvt_pk_bf16_f32 v27, v27, v27
	ds_write_b16 v66, v27 offset:4864
	v_mul_f32_e32 v43, v43, v81
	v_cvt_pk_bf16_f32 v43, v43, v43
	ds_write_b16 v66, v43 offset:4928
	v_mul_f32_e32 v59, v59, v81
	v_cvt_pk_bf16_f32 v59, v59, v59
	ds_write_b16 v66, v59 offset:4992
	v_mul_f32_e32 v11, v11, v81
	v_cvt_pk_bf16_f32 v11, v11, v11
	ds_write_b16 v66, v11 offset:5056
	v_mul_f32_e32 v28, v28, v82
	v_cvt_pk_bf16_f32 v28, v28, v28
	ds_write_b16 v66, v28 offset:6144
	v_mul_f32_e32 v44, v44, v82
	v_cvt_pk_bf16_f32 v44, v44, v44
	ds_write_b16 v66, v44 offset:6208
	v_mul_f32_e32 v60, v60, v82
	v_cvt_pk_bf16_f32 v60, v60, v60
	ds_write_b16 v66, v60 offset:6272
	v_mul_f32_e32 v12, v12, v82
	v_cvt_pk_bf16_f32 v12, v12, v12
	ds_write_b16 v66, v12 offset:6336
	v_mul_f32_e32 v29, v29, v83
	v_cvt_pk_bf16_f32 v29, v29, v29
	ds_write_b16 v66, v29 offset:6400
	v_mul_f32_e32 v45, v45, v83
	v_cvt_pk_bf16_f32 v45, v45, v45
	ds_write_b16 v66, v45 offset:6464
	v_mul_f32_e32 v61, v61, v83
	v_cvt_pk_bf16_f32 v61, v61, v61
	ds_write_b16 v66, v61 offset:6528
	v_mul_f32_e32 v13, v13, v83
	v_cvt_pk_bf16_f32 v13, v13, v13
	ds_write_b16 v66, v13 offset:6592
	v_mul_f32_e32 v30, v30, v84
	v_cvt_pk_bf16_f32 v30, v30, v30
	ds_write_b16 v66, v30 offset:6656
	v_mul_f32_e32 v46, v46, v84
	v_cvt_pk_bf16_f32 v46, v46, v46
	ds_write_b16 v66, v46 offset:6720
	v_mul_f32_e32 v62, v62, v84
	v_cvt_pk_bf16_f32 v62, v62, v62
	ds_write_b16 v66, v62 offset:6784
	v_mul_f32_e32 v14, v14, v84
	v_cvt_pk_bf16_f32 v14, v14, v14
	ds_write_b16 v66, v14 offset:6848
	v_mul_f32_e32 v31, v31, v85
	v_cvt_pk_bf16_f32 v31, v31, v31
	ds_write_b16 v66, v31 offset:6912
	v_mul_f32_e32 v47, v47, v85
	v_cvt_pk_bf16_f32 v47, v47, v47
	ds_write_b16 v66, v47 offset:6976
	v_mul_f32_e32 v63, v63, v85
	v_cvt_pk_bf16_f32 v63, v63, v63
	ds_write_b16 v66, v63 offset:7040
	v_mul_f32_e32 v15, v15, v85
	v_cvt_pk_bf16_f32 v15, v15, v15
	ds_write_b16 v66, v15 offset:7104
	s_add_u32 s0, s6, 0x9100000
	s_addc_u32 s1, s7, 0
	s_cmp_lg_u32 s14, 0
	s_cselect_b64 s[6:7], -1, 0
	s_and_b64 vcc, exec, s[6:7]
	v_and_b32_e32 v6, 15, v154
	v_lshrrev_b32_e32 v7, 4, v155
	v_or_b32_e32 v4, s8, v7
	v_add_u32_e32 v4, s9, v4
	v_ashrrev_i32_e32 v5, 31, v4
	v_lshlrev_b64 v[4:5], 10, v[4:5]
	v_lshl_add_u64 v[4:5], s[0:1], 0, v[4:5]
	v_lshl_add_u64 v[4:5], s[2:3], 1, v[4:5]
	v_lshlrev_b32_e32 v64, 4, v6
	v_add_u32_e32 v8, s4, v64
	v_lshl_add_u64 v[4:5], v[4:5], 0, v[64:65]
	s_waitcnt lgkmcnt(0)
	v_lshl_add_u32 v0, v7, 8, v8
	ds_read_b128 v[0:3], v0
	s_cbranch_vccz .LBB0_1260
	s_waitcnt lgkmcnt(0)
	global_store_dwordx4 v[4:5], v[0:3], off
	s_cbranch_execnz .LBB0_1219
